# speedup vs baseline: 1.0083x; 1.0083x over previous
.Lno_touch:
	s_waitcnt vmcnt(0)
.Lmask_ready:
	v_cmp_ne_u32_e64 s[4:5], 0, v12
	s_nop 1
	v_cndmask_b32_e64 v8, 0, 1, s[4:5]
	v_cmp_eq_u32_e64 s[4:5], 0, v13
	s_nop 1
	v_cndmask_b32_e64 v9, 2, 0, s[4:5]
	v_cmp_eq_u32_e64 s[4:5], 0, v14
	v_or_b32_e32 v8, v9, v8
	s_nop 0
	v_cndmask_b32_e64 v12, 4, 0, s[4:5]
	v_cmp_eq_u32_e64 s[4:5], 0, v15
	s_nop 1
	v_cndmask_b32_e64 v13, 8, 0, s[4:5]
	v_cmp_eq_u32_e64 s[4:5], 0, v16
	v_or3_b32 v8, v8, v12, v13
	s_nop 0
	v_cndmask_b32_e64 v14, 16, 0, s[4:5]
	v_cmp_eq_u32_e64 s[4:5], 0, v17
	s_nop 1
	v_cndmask_b32_e64 v15, 32, 0, s[4:5]
	v_cmp_eq_u32_e64 s[4:5], 0, v18
	s_nop 1
	v_cndmask_b32_e64 v16, 64, 0, s[4:5]
	v_cmp_eq_u32_e64 s[4:5], 0, v19
	s_nop 1
	v_cndmask_b32_e64 v7, v7, 0, s[4:5]
	v_or_b32_e32 v7, v16, v7
	v_or3_b32 v9, v7, v15, v14
	v_or_b32_e32 v7, v9, v8
	v_bcnt_u32_b32 v8, v8, 0
	v_bcnt_u32_b32 v9, v9, 0
	v_lshl_or_b32 v9, v9, 16, v8
	v_cmp_ne_u32_e64 s[4:5], 0, v7
	s_nop 0
	v_add_u32_dpp v8, v9, v9 row_shr:1 row_mask:0xf bank_mask:0xf bound_ctrl:1
	s_nop 1
	v_add_u32_dpp v8, v8, v8 row_shr:2 row_mask:0xf bank_mask:0xf bound_ctrl:1
	s_nop 1
	v_add_u32_dpp v8, v8, v8 row_shr:4 row_mask:0xf bank_mask:0xf bound_ctrl:1
	s_nop 1
	v_add_u32_dpp v12, v8, v8 row_shr:8 row_mask:0xf bank_mask:0xf bound_ctrl:1
	s_nop 1
	v_add_u32_dpp v12, v12, v12 row_bcast:15 row_mask:0xa bank_mask:0xf
	s_nop 1
	v_add_u32_dpp v12, v12, v12 row_bcast:31 row_mask:0xc bank_mask:0xf
	s_nop 0
	v_readlane_b32 s14, v12, 63
	s_and_b32 s3, s14, 0xffff
	s_and_saveexec_b64 s[10:11], s[4:5]
	s_cbranch_execz .LBB0_5
	v_sub_u32_e32 v12, v12, v9
	v_lshlrev_b32_e32 v8, 10, v1
	v_add_u32_sdwa v9, sext(v12), s3 dst_sel:DWORD dst_unused:UNUSED_PAD src0_sel:WORD_1 src1_sel:DWORD
	v_and_b32_e32 v12, 0xffff, v12
	v_lshlrev_b32_e32 v13, 2, v10
	s_mov_b64 s[12:13], 0
	v_mov_b32_e32 v14, 0x100

.LBB0_5:
	s_or_b64 exec, exec, s[10:11]
	s_and_saveexec_b64 s[0:1], vcc
	ds_write_b128 v11, v[2:5] offset:16384
	s_or_b64 exec, exec, s[0:1]
	s_ashr_i32 s0, s14, 16
	s_add_i32 s3, s3, s0
	v_cmp_gt_i32_e32 vcc, s3, v10
	v_mov_b32_e32 v2, 0
	s_waitcnt lgkmcnt(0)
	s_sub_u32 s26, 0x1ff, s2
	s_lshr_b32 s26, s26, 3
	s_min_u32 s26, s26, 64
	s_cmp_eq_u32 s26, 0
	s_cbranch_scc1 .Lhold_done

.Lhold_done:
	s_and_saveexec_b64 s[0:1], vcc
	s_cbranch_execz .Lmid_bar
	v_lshlrev_b32_e32 v3, 1, v10
	v_lshl_or_b32 v3, v1, 10, v3
	v_mov_b32_e32 v4, v10
	ds_read_u16 v5, v3
	s_waitcnt lgkmcnt(0)
	v_add_u32_e32 v8, v6, v5
	v_lshlrev_b32_e32 v8, 4, v8
	global_load_dwordx4 v[12:15], v8, s[16:17] nt
	global_load_dwordx4 v[16:19], v8, s[18:19] nt
	v_lshlrev_b32_e32 v5, 4, v5
